# v43 + MoE weight conversion items: 128 per-item 64-bit VALU address ops replaced by SGPR base stepping + one per-lane offset (4 item instances)
# baseline (speedup 1.0000x reference)
.LBB0_361:
	v_mov_b32_e32 v6, v172
	s_cmpk_gt_u32 s20, 0x7fff
	s_mov_b64 s[0:1], -1
	s_cbranch_scc0 .LBB0_363
	s_add_i32 s0, s20, 0xffff8000
	s_lshr_b32 s8, s0, 9
	s_lshl_b64 s[0:1], s[8:9], 20
	s_lshl_b64 s[74:75], s[8:9], 22
	s_add_u32 s76, s14, s74
	s_addc_u32 s75, s15, s75
	s_add_u32 s0, s26, s0
	s_addc_u32 s1, s27, s1
	s_add_i32 s8, s21, s23
	s_and_b32 s8, s8, 0x3c0
	s_and_b32 s74, s22, 0x3e0
	v_ashrrev_i32_e32 v7, 5, v6
	s_lshl_b32 s77, s74, 2
	v_add_u32_e32 v4, s8, v7
	v_and_b32_e32 v24, 31, v6
	s_add_u32 s76, s76, s77
	s_addc_u32 s77, s75, 0
	v_lshlrev_b32_e32 v0, 2, v24
	v_lshl_add_u32 v2, v7, 12, v0
	s_lshl_b32 s98, s8, 12
	s_add_u32 s100, s76, s98
	s_addc_u32 s101, s77, 0
	global_load_dword v25, v2, s[100:101]
	s_add_u32 s100, s100, 0x2000
	s_addc_u32 s101, s101, 0
	global_load_dword v26, v2, s[100:101]
	s_add_u32 s100, s100, 0x2000
	s_addc_u32 s101, s101, 0
	global_load_dword v27, v2, s[100:101]
	s_add_u32 s100, s100, 0x2000
	s_addc_u32 s101, s101, 0
	global_load_dword v28, v2, s[100:101]
	s_add_u32 s100, s100, 0x2000
	s_addc_u32 s101, s101, 0
	global_load_dword v29, v2, s[100:101]
	s_add_u32 s100, s100, 0x2000
	s_addc_u32 s101, s101, 0
	global_load_dword v30, v2, s[100:101]
	s_add_u32 s100, s100, 0x2000
	s_addc_u32 s101, s101, 0
	global_load_dword v31, v2, s[100:101]
	s_add_u32 s100, s100, 0x2000
	s_addc_u32 s101, s101, 0
	global_load_dword v32, v2, s[100:101]
	s_add_u32 s100, s100, 0x2000
	s_addc_u32 s101, s101, 0
	global_load_dword v33, v2, s[100:101]
	s_add_u32 s100, s100, 0x2000
	s_addc_u32 s101, s101, 0
	global_load_dword v34, v2, s[100:101]
	s_add_u32 s100, s100, 0x2000
	s_addc_u32 s101, s101, 0
	global_load_dword v35, v2, s[100:101]
	s_add_u32 s100, s100, 0x2000
	s_addc_u32 s101, s101, 0
	global_load_dword v36, v2, s[100:101]
	s_add_u32 s100, s100, 0x2000
	s_addc_u32 s101, s101, 0
	global_load_dword v37, v2, s[100:101]
	s_add_u32 s100, s100, 0x2000
	s_addc_u32 s101, s101, 0
	global_load_dword v38, v2, s[100:101]
	s_add_u32 s100, s100, 0x2000
	s_addc_u32 s101, s101, 0
	global_load_dword v39, v2, s[100:101]
	s_add_u32 s100, s100, 0x2000
	s_addc_u32 s101, s101, 0
	global_load_dword v40, v2, s[100:101]
	s_add_u32 s100, s100, 0x2000
	s_addc_u32 s101, s101, 0
	global_load_dword v41, v2, s[100:101]
	s_add_u32 s100, s100, 0x2000
	s_addc_u32 s101, s101, 0
	global_load_dword v42, v2, s[100:101]
	s_add_u32 s100, s100, 0x2000
	s_addc_u32 s101, s101, 0
	global_load_dword v43, v2, s[100:101]
	s_add_u32 s100, s100, 0x2000
	s_addc_u32 s101, s101, 0
	global_load_dword v44, v2, s[100:101]
	s_add_u32 s100, s100, 0x2000
	s_addc_u32 s101, s101, 0
	global_load_dword v45, v2, s[100:101]
	s_add_u32 s100, s100, 0x2000
	s_addc_u32 s101, s101, 0
	global_load_dword v46, v2, s[100:101]
	s_add_u32 s100, s100, 0x2000
	s_addc_u32 s101, s101, 0
	global_load_dword v20, v2, s[100:101]
	s_add_u32 s100, s100, 0x2000
	s_addc_u32 s101, s101, 0
	global_load_dword v21, v2, s[100:101]
	s_add_u32 s100, s100, 0x2000
	s_addc_u32 s101, s101, 0
	global_load_dword v22, v2, s[100:101]
	s_add_u32 s100, s100, 0x2000
	s_addc_u32 s101, s101, 0
	global_load_dword v10, v2, s[100:101]
	s_add_u32 s100, s100, 0x2000
	s_addc_u32 s101, s101, 0
	global_load_dword v11, v2, s[100:101]
	s_add_u32 s100, s100, 0x2000
	s_addc_u32 s101, s101, 0
	global_load_dword v12, v2, s[100:101]
	s_add_u32 s100, s100, 0x2000
	s_addc_u32 s101, s101, 0
	global_load_dword v13, v2, s[100:101]
	s_add_u32 s100, s100, 0x2000
	s_addc_u32 s101, s101, 0
	global_load_dword v14, v2, s[100:101]
	s_add_u32 s100, s100, 0x2000
	s_addc_u32 s101, s101, 0
	global_load_dword v4, v2, s[100:101]
	s_add_u32 s100, s100, 0x2000
	s_addc_u32 s101, s101, 0
	global_load_dword v5, v2, s[100:101]
	v_add_u32_e32 v0, s24, v0
	v_mad_u64_u32 v[2:3], s[76:77], v7, s72, v[0:1]
	s_waitcnt vmcnt(0)
	v_mul_f32_e32 v8, 0x42800000, v25
	v_mul_f32_e32 v3, 0x42800000, v26
	ds_write2_b32 v2, v8, v3 offset1:66
	v_mul_f32_e32 v3, 0x42800000, v27
	v_mul_f32_e32 v7, 0x42800000, v28
	ds_write2_b32 v2, v3, v7 offset0:132 offset1:198
	v_mul_f32_e32 v3, 0x42800000, v29
	v_mul_f32_e32 v7, 0x42800000, v30
	v_add_u32_e32 v8, 0x400, v2
	ds_write2_b32 v8, v3, v7 offset0:8 offset1:74
	v_mul_f32_e32 v3, 0x42800000, v31
	v_mul_f32_e32 v7, 0x42800000, v32
	ds_write2_b32 v8, v3, v7 offset0:140 offset1:206
	v_mul_f32_e32 v3, 0x42800000, v33
	v_mul_f32_e32 v7, 0x42800000, v34
	v_add_u32_e32 v8, 0x800, v2
	ds_write2_b32 v8, v3, v7 offset0:16 offset1:82
	v_mul_f32_e32 v3, 0x42800000, v35
	v_mul_f32_e32 v7, 0x42800000, v36
	ds_write2_b32 v8, v3, v7 offset0:148 offset1:214
	v_mul_f32_e32 v3, 0x42800000, v37
	v_mul_f32_e32 v7, 0x42800000, v38
	v_add_u32_e32 v8, 0xc00, v2
	ds_write2_b32 v8, v3, v7 offset0:24 offset1:90
	v_mul_f32_e32 v3, 0x42800000, v39
	v_mul_f32_e32 v7, 0x42800000, v40
	ds_write2_b32 v8, v3, v7 offset0:156 offset1:222
	v_add_u32_e32 v8, 0x1000, v2
	v_mul_f32_e32 v3, 0x42800000, v41
	v_mul_f32_e32 v7, 0x42800000, v42
	ds_write2_b32 v8, v3, v7 offset0:32 offset1:98
	v_mul_f32_e32 v3, 0x42800000, v43
	v_mul_f32_e32 v7, 0x42800000, v44
	ds_write2_b32 v8, v3, v7 offset0:164 offset1:230
	v_mul_f32_e32 v3, 0x42800000, v45
	v_mul_f32_e32 v7, 0x42800000, v46
	v_add_u32_e32 v8, 0x1400, v2
	ds_write2_b32 v8, v3, v7 offset0:40 offset1:106
	v_mul_f32_e32 v3, 0x42800000, v20
	v_mul_f32_e32 v7, 0x42800000, v21
	ds_write2_b32 v8, v3, v7 offset0:172 offset1:238
	v_add_u32_e32 v8, 0x1800, v2
	v_add_u32_e32 v2, 0x1c00, v2
	v_mul_f32_e32 v3, 0x42800000, v22
	v_mul_f32_e32 v7, 0x42800000, v10
	ds_write2_b32 v8, v3, v7 offset0:48 offset1:114
	v_mul_f32_e32 v3, 0x42800000, v11
	v_mul_f32_e32 v7, 0x42800000, v12
	ds_write2_b32 v8, v3, v7 offset0:180 offset1:246
	v_mul_f32_e32 v3, 0x42800000, v13
	v_mul_f32_e32 v7, 0x42800000, v14
	ds_write2_b32 v2, v3, v7 offset0:56 offset1:122
	v_and_b32_e32 v12, 0xffffffe0, v6
	v_mad_u64_u32 v[10:11], s[76:77], v12, s72, v[0:1]
	v_mul_f32_e32 v3, 0x42800000, v4
	v_mul_f32_e32 v4, 0x42800000, v5
	ds_write2_b32 v2, v3, v4 offset0:188 offset1:254
	s_waitcnt lgkmcnt(0)
	ds_read2_b32 v[2:3], v10 offset1:33
	ds_read2_b32 v[4:5], v10 offset0:66 offset1:99
	ds_read2_b32 v[8:9], v10 offset0:132 offset1:165
	s_waitcnt lgkmcnt(2)
	v_med3_f32 v0, v2, s73, v188
	v_med3_f32 v3, v3, s73, v188
	v_mov_b32_e32 v2, v1
	v_cvt_pk_fp8_f32 v2, v0, v3
	s_waitcnt lgkmcnt(1)
	v_med3_f32 v0, v4, s73, v188
	v_med3_f32 v3, v5, s73, v188
	s_waitcnt lgkmcnt(0)
	v_med3_f32 v7, v9, s73, v188
	v_cvt_pk_fp8_f32 v2, v0, v3 op_sel:[0,0,1]
	v_med3_f32 v0, v8, s73, v188
	v_mov_b32_e32 v3, v1
	ds_read2_b32 v[4:5], v10 offset0:198 offset1:231
	v_cvt_pk_fp8_f32 v3, v0, v7
	v_add_u32_e32 v0, 0x400, v10
	ds_read2_b32 v[8:9], v0 offset0:8 offset1:41
	ds_read2_b32 v[14:15], v0 offset0:74 offset1:107
	s_waitcnt lgkmcnt(2)
	v_med3_f32 v4, v4, s73, v188
	v_med3_f32 v5, v5, s73, v188
	v_cvt_pk_fp8_f32 v3, v4, v5 op_sel:[0,0,1]
	s_waitcnt lgkmcnt(1)
	v_med3_f32 v5, v8, s73, v188
	v_med3_f32 v7, v9, s73, v188
	v_mov_b32_e32 v4, v1
	ds_read2_b32 v[8:9], v0 offset0:140 offset1:173
	v_cvt_pk_fp8_f32 v4, v5, v7
	s_waitcnt lgkmcnt(1)
	v_med3_f32 v5, v14, s73, v188
	v_med3_f32 v7, v15, s73, v188
	ds_read2_b32 v[14:15], v0 offset0:206 offset1:239
	v_cvt_pk_fp8_f32 v4, v5, v7 op_sel:[0,0,1]
	s_waitcnt lgkmcnt(1)
	v_med3_f32 v0, v8, s73, v188
	v_med3_f32 v7, v9, s73, v188
	v_mov_b32_e32 v5, v1
	v_cvt_pk_fp8_f32 v5, v0, v7
	v_add_u32_e32 v0, 0x800, v10
	ds_read2_b32 v[8:9], v0 offset0:16 offset1:49
	s_waitcnt lgkmcnt(1)
	v_med3_f32 v7, v14, s73, v188
	v_med3_f32 v11, v15, s73, v188
	ds_read2_b32 v[14:15], v0 offset0:82 offset1:115
	v_cvt_pk_fp8_f32 v5, v7, v11 op_sel:[0,0,1]
	s_waitcnt lgkmcnt(1)
	v_med3_f32 v7, v8, s73, v188
	v_med3_f32 v9, v9, s73, v188
	v_mov_b32_e32 v8, v1
	ds_read2_b32 v[16:17], v0 offset0:148 offset1:181
	v_cvt_pk_fp8_f32 v8, v7, v9
	s_waitcnt lgkmcnt(1)
	v_med3_f32 v7, v14, s73, v188
	v_med3_f32 v9, v15, s73, v188
	ds_read2_b32 v[14:15], v0 offset0:214 offset1:247
	v_cvt_pk_fp8_f32 v8, v7, v9 op_sel:[0,0,1]
	s_waitcnt lgkmcnt(1)
	v_med3_f32 v0, v16, s73, v188
	v_med3_f32 v7, v17, s73, v188
	v_mov_b32_e32 v9, v1
	v_cvt_pk_fp8_f32 v9, v0, v7
	v_add_u32_e32 v0, 0xc00, v10
	ds_read2_b32 v[10:11], v0 offset0:24 offset1:57
	ds_read2_b32 v[16:17], v0 offset0:90 offset1:123
	s_waitcnt lgkmcnt(2)
	v_med3_f32 v7, v14, s73, v188
	v_med3_f32 v13, v15, s73, v188
	ds_read2_b32 v[14:15], v0 offset0:156 offset1:189
	v_cvt_pk_fp8_f32 v9, v7, v13 op_sel:[0,0,1]
	s_waitcnt lgkmcnt(2)
	v_med3_f32 v7, v10, s73, v188
	v_med3_f32 v11, v11, s73, v188
	s_waitcnt lgkmcnt(1)
	v_med3_f32 v13, v16, s73, v188
	v_med3_f32 v18, v17, s73, v188
	v_mov_b32_e32 v10, v1
	ds_read2_b32 v[16:17], v0 offset0:222 offset1:255
	v_cvt_pk_fp8_f32 v10, v7, v11
	s_waitcnt lgkmcnt(1)
	v_med3_f32 v0, v14, s73, v188
	v_med3_f32 v7, v15, s73, v188
	v_mov_b32_e32 v11, v1
	v_cvt_pk_fp8_f32 v11, v0, v7
	s_waitcnt lgkmcnt(0)
	v_med3_f32 v0, v16, s73, v188
	v_med3_f32 v7, v17, s73, v188
	v_cvt_pk_fp8_f32 v10, v13, v18 op_sel:[0,0,1]
	v_cvt_pk_fp8_f32 v11, v0, v7 op_sel:[0,0,1]
	v_or_b32_e32 v0, s74, v24
	v_lshlrev_b32_e32 v0, 10, v0
	v_lshl_add_u64 v[14:15], s[0:1], 0, v[0:1]
	v_lshl_add_u64 v[14:15], v[14:15], 0, s[8:9]
	v_ashrrev_i32_e32 v13, 31, v12
	v_lshl_add_u64 v[12:13], v[14:15], 0, v[12:13]
	global_store_dwordx4 v[12:13], v[2:5], off
	global_store_dwordx4 v[12:13], v[8:11], off offset:16
	s_waitcnt lgkmcnt(0)
	s_mov_b64 s[0:1], 0
.LBB0_363:
	s_andn2_b64 vcc, exec, s[0:1]
	s_cbranch_vccnz .LBB0_360
	s_lshr_b32 s8, s20, 10
	s_lshl_b64 s[0:1], s[8:9], 23
	s_add_u32 s75, s12, s0
	s_addc_u32 s77, s13, s1
	s_lshl_b64 s[0:1], s[8:9], 21
	s_add_u32 s0, s28, s0
	s_addc_u32 s1, s29, s1
	s_and_b32 s8, s20, 0x3c0
	s_and_b32 s74, s22, 0x7e0
	v_ashrrev_i32_e32 v7, 5, v6
	s_lshl_b32 s76, s74, 2
	v_add_u32_e32 v4, s8, v7
	v_and_b32_e32 v24, 31, v6
	s_add_u32 s76, s75, s76
	s_addc_u32 s77, s77, 0
	v_lshlrev_b32_e32 v0, 2, v24
	v_lshl_add_u32 v2, v7, 13, v0
	s_lshl_b32 s98, s8, 13
	s_add_u32 s100, s76, s98
	s_addc_u32 s101, s77, 0
	global_load_dword v25, v2, s[100:101]
	s_add_u32 s100, s100, 0x4000
	s_addc_u32 s101, s101, 0
	global_load_dword v26, v2, s[100:101]
	s_add_u32 s100, s100, 0x4000
	s_addc_u32 s101, s101, 0
	global_load_dword v27, v2, s[100:101]
	s_add_u32 s100, s100, 0x4000
	s_addc_u32 s101, s101, 0
	global_load_dword v28, v2, s[100:101]
	s_add_u32 s100, s100, 0x4000
	s_addc_u32 s101, s101, 0
	global_load_dword v29, v2, s[100:101]
	s_add_u32 s100, s100, 0x4000
	s_addc_u32 s101, s101, 0
	global_load_dword v30, v2, s[100:101]
	s_add_u32 s100, s100, 0x4000
	s_addc_u32 s101, s101, 0
	global_load_dword v31, v2, s[100:101]
	s_add_u32 s100, s100, 0x4000
	s_addc_u32 s101, s101, 0
	global_load_dword v32, v2, s[100:101]
	s_add_u32 s100, s100, 0x4000
	s_addc_u32 s101, s101, 0
	global_load_dword v33, v2, s[100:101]
	s_add_u32 s100, s100, 0x4000
	s_addc_u32 s101, s101, 0
	global_load_dword v34, v2, s[100:101]
	s_add_u32 s100, s100, 0x4000
	s_addc_u32 s101, s101, 0
	global_load_dword v35, v2, s[100:101]
	s_add_u32 s100, s100, 0x4000
	s_addc_u32 s101, s101, 0
	global_load_dword v36, v2, s[100:101]
	s_add_u32 s100, s100, 0x4000
	s_addc_u32 s101, s101, 0
	global_load_dword v37, v2, s[100:101]
	s_add_u32 s100, s100, 0x4000
	s_addc_u32 s101, s101, 0
	global_load_dword v38, v2, s[100:101]
	s_add_u32 s100, s100, 0x4000
	s_addc_u32 s101, s101, 0
	global_load_dword v39, v2, s[100:101]
	s_add_u32 s100, s100, 0x4000
	s_addc_u32 s101, s101, 0
	global_load_dword v40, v2, s[100:101]
	s_add_u32 s100, s100, 0x4000
	s_addc_u32 s101, s101, 0
	global_load_dword v41, v2, s[100:101]
	s_add_u32 s100, s100, 0x4000
	s_addc_u32 s101, s101, 0
	global_load_dword v42, v2, s[100:101]
	s_add_u32 s100, s100, 0x4000
	s_addc_u32 s101, s101, 0
	global_load_dword v43, v2, s[100:101]
	s_add_u32 s100, s100, 0x4000
	s_addc_u32 s101, s101, 0
	global_load_dword v44, v2, s[100:101]
	s_add_u32 s100, s100, 0x4000
	s_addc_u32 s101, s101, 0
	global_load_dword v45, v2, s[100:101]
	s_add_u32 s100, s100, 0x4000
	s_addc_u32 s101, s101, 0
	global_load_dword v46, v2, s[100:101]
	s_add_u32 s100, s100, 0x4000
	s_addc_u32 s101, s101, 0
	global_load_dword v20, v2, s[100:101]
	s_add_u32 s100, s100, 0x4000
	s_addc_u32 s101, s101, 0
	global_load_dword v21, v2, s[100:101]
	s_add_u32 s100, s100, 0x4000
	s_addc_u32 s101, s101, 0
	global_load_dword v22, v2, s[100:101]
	s_add_u32 s100, s100, 0x4000
	s_addc_u32 s101, s101, 0
	global_load_dword v10, v2, s[100:101]
	s_add_u32 s100, s100, 0x4000
	s_addc_u32 s101, s101, 0
	global_load_dword v11, v2, s[100:101]
	s_add_u32 s100, s100, 0x4000
	s_addc_u32 s101, s101, 0
	global_load_dword v12, v2, s[100:101]
	s_add_u32 s100, s100, 0x4000
	s_addc_u32 s101, s101, 0
	global_load_dword v13, v2, s[100:101]
	s_add_u32 s100, s100, 0x4000
	s_addc_u32 s101, s101, 0
	global_load_dword v14, v2, s[100:101]
	s_add_u32 s100, s100, 0x4000
	s_addc_u32 s101, s101, 0
	global_load_dword v4, v2, s[100:101]
	s_add_u32 s100, s100, 0x4000
	s_addc_u32 s101, s101, 0
	global_load_dword v5, v2, s[100:101]
	v_add_u32_e32 v0, s24, v0
	v_mad_u64_u32 v[2:3], s[76:77], v7, s72, v[0:1]
	s_waitcnt vmcnt(0)
	v_mul_f32_e32 v8, 0x42800000, v25
	v_mul_f32_e32 v3, 0x42800000, v26
	ds_write2_b32 v2, v8, v3 offset1:66
	v_mul_f32_e32 v3, 0x42800000, v27
	v_mul_f32_e32 v7, 0x42800000, v28
	ds_write2_b32 v2, v3, v7 offset0:132 offset1:198
	v_mul_f32_e32 v3, 0x42800000, v29
	v_mul_f32_e32 v7, 0x42800000, v30
	v_add_u32_e32 v8, 0x400, v2
	ds_write2_b32 v8, v3, v7 offset0:8 offset1:74
	v_mul_f32_e32 v3, 0x42800000, v31
	v_mul_f32_e32 v7, 0x42800000, v32
	ds_write2_b32 v8, v3, v7 offset0:140 offset1:206
	v_mul_f32_e32 v3, 0x42800000, v33
	v_mul_f32_e32 v7, 0x42800000, v34
	v_add_u32_e32 v8, 0x800, v2
	ds_write2_b32 v8, v3, v7 offset0:16 offset1:82
	v_mul_f32_e32 v3, 0x42800000, v35
	v_mul_f32_e32 v7, 0x42800000, v36
	ds_write2_b32 v8, v3, v7 offset0:148 offset1:214
	v_mul_f32_e32 v3, 0x42800000, v37
	v_mul_f32_e32 v7, 0x42800000, v38
	v_add_u32_e32 v8, 0xc00, v2
	ds_write2_b32 v8, v3, v7 offset0:24 offset1:90
	v_mul_f32_e32 v3, 0x42800000, v39
	v_mul_f32_e32 v7, 0x42800000, v40
	ds_write2_b32 v8, v3, v7 offset0:156 offset1:222
	v_add_u32_e32 v8, 0x1000, v2
	v_mul_f32_e32 v3, 0x42800000, v41
	v_mul_f32_e32 v7, 0x42800000, v42
	ds_write2_b32 v8, v3, v7 offset0:32 offset1:98
	v_mul_f32_e32 v3, 0x42800000, v43
	v_mul_f32_e32 v7, 0x42800000, v44
	ds_write2_b32 v8, v3, v7 offset0:164 offset1:230
	v_mul_f32_e32 v3, 0x42800000, v45
	v_mul_f32_e32 v7, 0x42800000, v46
	v_add_u32_e32 v8, 0x1400, v2
	ds_write2_b32 v8, v3, v7 offset0:40 offset1:106
	v_mul_f32_e32 v3, 0x42800000, v20
	v_mul_f32_e32 v7, 0x42800000, v21
	ds_write2_b32 v8, v3, v7 offset0:172 offset1:238
	v_add_u32_e32 v8, 0x1800, v2
	v_add_u32_e32 v2, 0x1c00, v2
	v_mul_f32_e32 v3, 0x42800000, v22
	v_mul_f32_e32 v7, 0x42800000, v10
	ds_write2_b32 v8, v3, v7 offset0:48 offset1:114
	v_mul_f32_e32 v3, 0x42800000, v11
	v_mul_f32_e32 v7, 0x42800000, v12
	ds_write2_b32 v8, v3, v7 offset0:180 offset1:246
	v_mul_f32_e32 v3, 0x42800000, v13
	v_mul_f32_e32 v7, 0x42800000, v14
	ds_write2_b32 v2, v3, v7 offset0:56 offset1:122
	v_and_b32_e32 v10, 0xffffffe0, v6
	v_mad_u64_u32 v[8:9], s[76:77], v10, s72, v[0:1]
	v_mul_f32_e32 v3, 0x42800000, v4
	v_mul_f32_e32 v4, 0x42800000, v5
	ds_write2_b32 v2, v3, v4 offset0:188 offset1:254
	s_waitcnt lgkmcnt(0)
	ds_read2_b32 v[2:3], v8 offset1:33
	ds_read2_b32 v[4:5], v8 offset0:66 offset1:99
	ds_read2_b32 v[6:7], v8 offset0:132 offset1:165
	s_waitcnt lgkmcnt(2)
	v_med3_f32 v0, v2, s73, v188
	v_med3_f32 v3, v3, s73, v188
	v_mov_b32_e32 v2, v1
	v_cvt_pk_fp8_f32 v2, v0, v3
	s_waitcnt lgkmcnt(1)
	v_med3_f32 v0, v4, s73, v188
	v_med3_f32 v3, v5, s73, v188
	ds_read2_b32 v[4:5], v8 offset0:198 offset1:231
	v_cvt_pk_fp8_f32 v2, v0, v3 op_sel:[0,0,1]
	s_waitcnt lgkmcnt(1)
	v_med3_f32 v0, v6, s73, v188
	v_med3_f32 v6, v7, s73, v188
	v_mov_b32_e32 v3, v1
	v_cvt_pk_fp8_f32 v3, v0, v6
	v_add_u32_e32 v0, 0x400, v8
	ds_read2_b32 v[6:7], v0 offset0:8 offset1:41
	s_waitcnt lgkmcnt(1)
	v_med3_f32 v4, v4, s73, v188
	v_med3_f32 v5, v5, s73, v188
	v_cvt_pk_fp8_f32 v3, v4, v5 op_sel:[0,0,1]
	ds_read2_b32 v[12:13], v0 offset0:74 offset1:107
	s_waitcnt lgkmcnt(1)
	v_med3_f32 v5, v6, s73, v188
	v_med3_f32 v6, v7, s73, v188
	v_mov_b32_e32 v4, v1
	v_cvt_pk_fp8_f32 v4, v5, v6
	ds_read2_b32 v[6:7], v0 offset0:140 offset1:173
	s_waitcnt lgkmcnt(1)
	v_med3_f32 v5, v12, s73, v188
	v_med3_f32 v9, v13, s73, v188
	v_cvt_pk_fp8_f32 v4, v5, v9 op_sel:[0,0,1]
	ds_read2_b32 v[12:13], v0 offset0:206 offset1:239
	s_waitcnt lgkmcnt(1)
	v_med3_f32 v0, v6, s73, v188
	v_med3_f32 v6, v7, s73, v188
	v_mov_b32_e32 v5, v1
	v_cvt_pk_fp8_f32 v5, v0, v6
	v_add_u32_e32 v0, 0x800, v8
	ds_read2_b32 v[6:7], v0 offset0:16 offset1:49
	s_waitcnt lgkmcnt(1)
	v_med3_f32 v9, v12, s73, v188
	v_med3_f32 v11, v13, s73, v188
	ds_read2_b32 v[12:13], v0 offset0:82 offset1:115
	v_cvt_pk_fp8_f32 v5, v9, v11 op_sel:[0,0,1]
	s_waitcnt lgkmcnt(1)
	v_med3_f32 v9, v6, s73, v188
	v_med3_f32 v7, v7, s73, v188
	v_mov_b32_e32 v6, v1
	ds_read2_b32 v[14:15], v0 offset0:148 offset1:181
	v_cvt_pk_fp8_f32 v6, v9, v7
	s_waitcnt lgkmcnt(1)
	v_med3_f32 v7, v12, s73, v188
	v_med3_f32 v9, v13, s73, v188
	ds_read2_b32 v[12:13], v0 offset0:214 offset1:247
	v_cvt_pk_fp8_f32 v6, v7, v9 op_sel:[0,0,1]
	s_waitcnt lgkmcnt(1)
	v_med3_f32 v0, v14, s73, v188
	v_med3_f32 v9, v15, s73, v188
	v_mov_b32_e32 v7, v1
	v_cvt_pk_fp8_f32 v7, v0, v9
	v_add_u32_e32 v0, 0xc00, v8
	ds_read2_b32 v[8:9], v0 offset0:24 offset1:57
	s_waitcnt lgkmcnt(1)
	v_med3_f32 v11, v12, s73, v188
	ds_read2_b32 v[14:15], v0 offset0:90 offset1:123
	v_med3_f32 v12, v13, s73, v188
	v_cvt_pk_fp8_f32 v7, v11, v12 op_sel:[0,0,1]
	ds_read2_b32 v[12:13], v0 offset0:156 offset1:189
	s_waitcnt lgkmcnt(2)
	v_med3_f32 v11, v8, s73, v188
	v_med3_f32 v9, v9, s73, v188
	s_waitcnt lgkmcnt(1)
	v_med3_f32 v16, v14, s73, v188
	v_med3_f32 v17, v15, s73, v188
	v_mov_b32_e32 v8, v1
	ds_read2_b32 v[14:15], v0 offset0:222 offset1:255
	v_cvt_pk_fp8_f32 v8, v11, v9
	s_waitcnt lgkmcnt(1)
	v_med3_f32 v0, v12, s73, v188
	v_med3_f32 v11, v13, s73, v188
	v_mov_b32_e32 v9, v1
	v_cvt_pk_fp8_f32 v9, v0, v11
	s_waitcnt lgkmcnt(0)
	v_med3_f32 v0, v14, s73, v188
	v_med3_f32 v11, v15, s73, v188
	v_cvt_pk_fp8_f32 v8, v16, v17 op_sel:[0,0,1]
	v_cvt_pk_fp8_f32 v9, v0, v11 op_sel:[0,0,1]
	v_or_b32_e32 v0, s74, v24
	v_lshlrev_b32_e32 v0, 10, v0
	v_lshl_add_u64 v[12:13], s[0:1], 0, v[0:1]
	v_lshl_add_u64 v[12:13], v[12:13], 0, s[8:9]
	v_ashrrev_i32_e32 v11, 31, v10
	v_lshl_add_u64 v[10:11], v[12:13], 0, v[10:11]
	global_store_dwordx4 v[10:11], v[2:5], off
	global_store_dwordx4 v[10:11], v[6:9], off offset:16
	s_waitcnt lgkmcnt(0)
	s_branch .LBB0_360

.LBB0_1473:
	v_mov_b32_e32 v6, v158
	s_cmp_gt_i32 s15, 0xbfff
	s_cbranch_scc1 .LBB0_1472
	s_cmpk_gt_i32 s15, 0x7fff
	s_mov_b64 s[2:3], -1
	s_cbranch_scc0 .LBB0_1476
	s_add_i32 s2, s15, 0xffff8000
	s_lshr_b32 s6, s2, 9
	s_lshl_b64 s[2:3], s[6:7], 20
	s_lshl_b64 s[18:19], s[6:7], 22
	s_add_u32 s20, s12, s18
	s_addc_u32 s19, s13, s19
	s_add_u32 s2, s33, s2
	s_addc_u32 s3, s34, s3
	s_and_b32 s6, s17, 0x3c0
	s_and_b32 s18, s44, 0x3e0
	v_ashrrev_i32_e32 v7, 5, v6
	s_lshl_b32 s21, s18, 2
	v_add_u32_e32 v4, s6, v7
	v_and_b32_e32 v24, 31, v6
	s_add_u32 s20, s20, s21
	s_addc_u32 s21, s19, 0
	v_lshlrev_b32_e32 v0, 2, v24
	v_lshl_add_u32 v2, v7, 12, v0
	s_lshl_b32 s98, s6, 12
	s_add_u32 s100, s20, s98
	s_addc_u32 s101, s21, 0
	global_load_dword v25, v2, s[100:101]
	s_add_u32 s100, s100, 0x2000
	s_addc_u32 s101, s101, 0
	global_load_dword v26, v2, s[100:101]
	s_add_u32 s100, s100, 0x2000
	s_addc_u32 s101, s101, 0
	global_load_dword v27, v2, s[100:101]
	s_add_u32 s100, s100, 0x2000
	s_addc_u32 s101, s101, 0
	global_load_dword v28, v2, s[100:101]
	s_add_u32 s100, s100, 0x2000
	s_addc_u32 s101, s101, 0
	global_load_dword v29, v2, s[100:101]
	s_add_u32 s100, s100, 0x2000
	s_addc_u32 s101, s101, 0
	global_load_dword v30, v2, s[100:101]
	s_add_u32 s100, s100, 0x2000
	s_addc_u32 s101, s101, 0
	global_load_dword v31, v2, s[100:101]
	s_add_u32 s100, s100, 0x2000
	s_addc_u32 s101, s101, 0
	global_load_dword v32, v2, s[100:101]
	s_add_u32 s100, s100, 0x2000
	s_addc_u32 s101, s101, 0
	global_load_dword v33, v2, s[100:101]
	s_add_u32 s100, s100, 0x2000
	s_addc_u32 s101, s101, 0
	global_load_dword v34, v2, s[100:101]
	s_add_u32 s100, s100, 0x2000
	s_addc_u32 s101, s101, 0
	global_load_dword v35, v2, s[100:101]
	s_add_u32 s100, s100, 0x2000
	s_addc_u32 s101, s101, 0
	global_load_dword v36, v2, s[100:101]
	s_add_u32 s100, s100, 0x2000
	s_addc_u32 s101, s101, 0
	global_load_dword v37, v2, s[100:101]
	s_add_u32 s100, s100, 0x2000
	s_addc_u32 s101, s101, 0
	global_load_dword v38, v2, s[100:101]
	s_add_u32 s100, s100, 0x2000
	s_addc_u32 s101, s101, 0
	global_load_dword v39, v2, s[100:101]
	s_add_u32 s100, s100, 0x2000
	s_addc_u32 s101, s101, 0
	global_load_dword v40, v2, s[100:101]
	s_add_u32 s100, s100, 0x2000
	s_addc_u32 s101, s101, 0
	global_load_dword v41, v2, s[100:101]
	s_add_u32 s100, s100, 0x2000
	s_addc_u32 s101, s101, 0
	global_load_dword v42, v2, s[100:101]
	s_add_u32 s100, s100, 0x2000
	s_addc_u32 s101, s101, 0
	global_load_dword v43, v2, s[100:101]
	s_add_u32 s100, s100, 0x2000
	s_addc_u32 s101, s101, 0
	global_load_dword v44, v2, s[100:101]
	s_add_u32 s100, s100, 0x2000
	s_addc_u32 s101, s101, 0
	global_load_dword v45, v2, s[100:101]
	s_add_u32 s100, s100, 0x2000
	s_addc_u32 s101, s101, 0
	global_load_dword v46, v2, s[100:101]
	s_add_u32 s100, s100, 0x2000
	s_addc_u32 s101, s101, 0
	global_load_dword v20, v2, s[100:101]
	s_add_u32 s100, s100, 0x2000
	s_addc_u32 s101, s101, 0
	global_load_dword v21, v2, s[100:101]
	s_add_u32 s100, s100, 0x2000
	s_addc_u32 s101, s101, 0
	global_load_dword v22, v2, s[100:101]
	s_add_u32 s100, s100, 0x2000
	s_addc_u32 s101, s101, 0
	global_load_dword v10, v2, s[100:101]
	s_add_u32 s100, s100, 0x2000
	s_addc_u32 s101, s101, 0
	global_load_dword v11, v2, s[100:101]
	s_add_u32 s100, s100, 0x2000
	s_addc_u32 s101, s101, 0
	global_load_dword v12, v2, s[100:101]
	s_add_u32 s100, s100, 0x2000
	s_addc_u32 s101, s101, 0
	global_load_dword v13, v2, s[100:101]
	s_add_u32 s100, s100, 0x2000
	s_addc_u32 s101, s101, 0
	global_load_dword v14, v2, s[100:101]
	s_add_u32 s100, s100, 0x2000
	s_addc_u32 s101, s101, 0
	global_load_dword v4, v2, s[100:101]
	s_add_u32 s100, s100, 0x2000
	s_addc_u32 s101, s101, 0
	global_load_dword v5, v2, s[100:101]
	v_add_u32_e32 v0, s23, v0
	v_mad_u64_u32 v[2:3], s[20:21], v7, s40, v[0:1]
	s_waitcnt vmcnt(31)
	v_mul_f32_e32 v8, 0x42800000, v25
	s_waitcnt vmcnt(30)
	v_mul_f32_e32 v3, 0x42800000, v26
	ds_write2_b32 v2, v8, v3 offset1:66
	s_waitcnt vmcnt(29)
	v_mul_f32_e32 v3, 0x42800000, v27
	s_waitcnt vmcnt(28)
	v_mul_f32_e32 v7, 0x42800000, v28
	ds_write2_b32 v2, v3, v7 offset0:132 offset1:198
	s_waitcnt vmcnt(27)
	v_mul_f32_e32 v3, 0x42800000, v29
	s_waitcnt vmcnt(26)
	v_mul_f32_e32 v7, 0x42800000, v30
	v_add_u32_e32 v8, 0x400, v2
	ds_write2_b32 v8, v3, v7 offset0:8 offset1:74
	s_waitcnt vmcnt(25)
	v_mul_f32_e32 v3, 0x42800000, v31
	s_waitcnt vmcnt(24)
	v_mul_f32_e32 v7, 0x42800000, v32
	ds_write2_b32 v8, v3, v7 offset0:140 offset1:206
	s_waitcnt vmcnt(23)
	v_mul_f32_e32 v3, 0x42800000, v33
	s_waitcnt vmcnt(22)
	v_mul_f32_e32 v7, 0x42800000, v34
	v_add_u32_e32 v8, 0x800, v2
	ds_write2_b32 v8, v3, v7 offset0:16 offset1:82
	s_waitcnt vmcnt(21)
	v_mul_f32_e32 v3, 0x42800000, v35
	s_waitcnt vmcnt(20)
	v_mul_f32_e32 v7, 0x42800000, v36
	ds_write2_b32 v8, v3, v7 offset0:148 offset1:214
	s_waitcnt vmcnt(19)
	v_mul_f32_e32 v3, 0x42800000, v37
	s_waitcnt vmcnt(18)
	v_mul_f32_e32 v7, 0x42800000, v38
	v_add_u32_e32 v8, 0xc00, v2
	ds_write2_b32 v8, v3, v7 offset0:24 offset1:90
	s_waitcnt vmcnt(17)
	v_mul_f32_e32 v3, 0x42800000, v39
	s_waitcnt vmcnt(16)
	v_mul_f32_e32 v7, 0x42800000, v40
	ds_write2_b32 v8, v3, v7 offset0:156 offset1:222
	v_add_u32_e32 v8, 0x1000, v2
	s_waitcnt vmcnt(15)
	v_mul_f32_e32 v3, 0x42800000, v41
	s_waitcnt vmcnt(14)
	v_mul_f32_e32 v7, 0x42800000, v42
	ds_write2_b32 v8, v3, v7 offset0:32 offset1:98
	s_waitcnt vmcnt(13)
	v_mul_f32_e32 v3, 0x42800000, v43
	s_waitcnt vmcnt(12)
	v_mul_f32_e32 v7, 0x42800000, v44
	ds_write2_b32 v8, v3, v7 offset0:164 offset1:230
	s_waitcnt vmcnt(11)
	v_mul_f32_e32 v3, 0x42800000, v45
	s_waitcnt vmcnt(10)
	v_mul_f32_e32 v7, 0x42800000, v46
	v_add_u32_e32 v8, 0x1400, v2
	ds_write2_b32 v8, v3, v7 offset0:40 offset1:106
	s_waitcnt vmcnt(9)
	v_mul_f32_e32 v3, 0x42800000, v20
	s_waitcnt vmcnt(8)
	v_mul_f32_e32 v7, 0x42800000, v21
	ds_write2_b32 v8, v3, v7 offset0:172 offset1:238
	v_add_u32_e32 v8, 0x1800, v2
	v_add_u32_e32 v2, 0x1c00, v2
	s_waitcnt vmcnt(7)
	v_mul_f32_e32 v3, 0x42800000, v22
	s_waitcnt vmcnt(6)
	v_mul_f32_e32 v7, 0x42800000, v10
	ds_write2_b32 v8, v3, v7 offset0:48 offset1:114
	s_waitcnt vmcnt(5)
	v_mul_f32_e32 v3, 0x42800000, v11
	s_waitcnt vmcnt(4)
	v_mul_f32_e32 v7, 0x42800000, v12
	ds_write2_b32 v8, v3, v7 offset0:180 offset1:246
	s_waitcnt vmcnt(3)
	v_mul_f32_e32 v3, 0x42800000, v13
	s_waitcnt vmcnt(2)
	v_mul_f32_e32 v7, 0x42800000, v14
	ds_write2_b32 v2, v3, v7 offset0:56 offset1:122
	v_and_b32_e32 v12, 0xffffffe0, v6
	v_mad_u64_u32 v[10:11], s[20:21], v12, s40, v[0:1]
	s_waitcnt vmcnt(1)
	v_mul_f32_e32 v3, 0x42800000, v4
	s_waitcnt vmcnt(0)
	v_mul_f32_e32 v4, 0x42800000, v5
	ds_write2_b32 v2, v3, v4 offset0:188 offset1:254
	s_waitcnt lgkmcnt(0)
	ds_read2_b32 v[2:3], v10 offset1:33
	ds_read2_b32 v[4:5], v10 offset0:66 offset1:99
	ds_read2_b32 v[8:9], v10 offset0:132 offset1:165
	s_waitcnt lgkmcnt(2)
	v_med3_f32 v0, v2, s39, v162
	v_med3_f32 v3, v3, s39, v162
	v_mov_b32_e32 v2, v1
	v_cvt_pk_fp8_f32 v2, v0, v3
	s_waitcnt lgkmcnt(1)
	v_med3_f32 v0, v4, s39, v162
	v_med3_f32 v3, v5, s39, v162
	s_waitcnt lgkmcnt(0)
	v_med3_f32 v7, v9, s39, v162
	v_cvt_pk_fp8_f32 v2, v0, v3 op_sel:[0,0,1]
	v_med3_f32 v0, v8, s39, v162
	v_mov_b32_e32 v3, v1
	ds_read2_b32 v[4:5], v10 offset0:198 offset1:231
	v_cvt_pk_fp8_f32 v3, v0, v7
	v_add_u32_e32 v0, 0x400, v10
	ds_read2_b32 v[8:9], v0 offset0:8 offset1:41
	ds_read2_b32 v[14:15], v0 offset0:74 offset1:107
	s_waitcnt lgkmcnt(2)
	v_med3_f32 v4, v4, s39, v162
	v_med3_f32 v5, v5, s39, v162
	v_cvt_pk_fp8_f32 v3, v4, v5 op_sel:[0,0,1]
	s_waitcnt lgkmcnt(1)
	v_med3_f32 v5, v8, s39, v162
	v_med3_f32 v7, v9, s39, v162
	v_mov_b32_e32 v4, v1
	ds_read2_b32 v[8:9], v0 offset0:140 offset1:173
	v_cvt_pk_fp8_f32 v4, v5, v7
	s_waitcnt lgkmcnt(1)
	v_med3_f32 v5, v14, s39, v162
	v_med3_f32 v7, v15, s39, v162
	ds_read2_b32 v[14:15], v0 offset0:206 offset1:239
	v_cvt_pk_fp8_f32 v4, v5, v7 op_sel:[0,0,1]
	s_waitcnt lgkmcnt(1)
	v_med3_f32 v0, v8, s39, v162
	v_med3_f32 v7, v9, s39, v162
	v_mov_b32_e32 v5, v1
	v_cvt_pk_fp8_f32 v5, v0, v7
	v_add_u32_e32 v0, 0x800, v10
	ds_read2_b32 v[8:9], v0 offset0:16 offset1:49
	s_waitcnt lgkmcnt(1)
	v_med3_f32 v7, v14, s39, v162
	v_med3_f32 v11, v15, s39, v162
	ds_read2_b32 v[14:15], v0 offset0:82 offset1:115
	v_cvt_pk_fp8_f32 v5, v7, v11 op_sel:[0,0,1]
	s_waitcnt lgkmcnt(1)
	v_med3_f32 v7, v8, s39, v162
	v_med3_f32 v9, v9, s39, v162
	v_mov_b32_e32 v8, v1
	ds_read2_b32 v[16:17], v0 offset0:148 offset1:181
	v_cvt_pk_fp8_f32 v8, v7, v9
	s_waitcnt lgkmcnt(1)
	v_med3_f32 v7, v14, s39, v162
	v_med3_f32 v9, v15, s39, v162
	ds_read2_b32 v[14:15], v0 offset0:214 offset1:247
	v_cvt_pk_fp8_f32 v8, v7, v9 op_sel:[0,0,1]
	s_waitcnt lgkmcnt(1)
	v_med3_f32 v0, v16, s39, v162
	v_med3_f32 v7, v17, s39, v162
	v_mov_b32_e32 v9, v1
	v_cvt_pk_fp8_f32 v9, v0, v7
	v_add_u32_e32 v0, 0xc00, v10
	ds_read2_b32 v[10:11], v0 offset0:24 offset1:57
	ds_read2_b32 v[16:17], v0 offset0:90 offset1:123
	s_waitcnt lgkmcnt(2)
	v_med3_f32 v7, v14, s39, v162
	v_med3_f32 v13, v15, s39, v162
	ds_read2_b32 v[14:15], v0 offset0:156 offset1:189
	v_cvt_pk_fp8_f32 v9, v7, v13 op_sel:[0,0,1]
	s_waitcnt lgkmcnt(2)
	v_med3_f32 v7, v10, s39, v162
	v_med3_f32 v11, v11, s39, v162
	s_waitcnt lgkmcnt(1)
	v_med3_f32 v13, v16, s39, v162
	v_med3_f32 v18, v17, s39, v162
	v_mov_b32_e32 v10, v1
	ds_read2_b32 v[16:17], v0 offset0:222 offset1:255
	v_cvt_pk_fp8_f32 v10, v7, v11
	s_waitcnt lgkmcnt(1)
	v_med3_f32 v0, v14, s39, v162
	v_med3_f32 v7, v15, s39, v162
	v_mov_b32_e32 v11, v1
	v_cvt_pk_fp8_f32 v11, v0, v7
	s_waitcnt lgkmcnt(0)
	v_med3_f32 v0, v16, s39, v162
	v_med3_f32 v7, v17, s39, v162
	v_cvt_pk_fp8_f32 v10, v13, v18 op_sel:[0,0,1]
	v_cvt_pk_fp8_f32 v11, v0, v7 op_sel:[0,0,1]
	v_or_b32_e32 v0, s18, v24
	v_lshlrev_b32_e32 v0, 10, v0
	v_lshl_add_u64 v[14:15], s[2:3], 0, v[0:1]
	v_lshl_add_u64 v[14:15], v[14:15], 0, s[6:7]
	v_ashrrev_i32_e32 v13, 31, v12
	v_lshl_add_u64 v[12:13], v[14:15], 0, v[12:13]
	global_store_dwordx4 v[12:13], v[2:5], off
	global_store_dwordx4 v[12:13], v[8:11], off offset:16
	s_waitcnt lgkmcnt(0)
	s_mov_b64 s[2:3], 0
.LBB0_1476:
	s_andn2_b64 vcc, exec, s[2:3]
	s_cbranch_vccnz .LBB0_1472
	s_ashr_i32 s2, s15, 31
	s_lshr_b32 s2, s2, 22
	s_add_i32 s3, s15, s2
	s_ashr_i32 s2, s3, 10
	s_and_b32 s3, s3, 0xfc00
	s_sub_i32 s6, s15, s3
	s_ashr_i32 s3, s2, 31
	s_lshl_b64 s[18:19], s[2:3], 23
	s_add_u32 s48, s10, s18
	s_addc_u32 s19, s11, s19
	s_lshl_b64 s[2:3], s[2:3], 21
	s_add_u32 s2, s35, s2
	s_sext_i32_i16 s18, s6
	s_addc_u32 s3, s36, s3
	s_bfe_u32 s18, s18, 0x60019
	s_add_i32 s18, s6, s18
	s_sext_i32_i16 s20, s18
	s_and_b32 s18, s18, 0xffc0
	s_sub_i32 s6, s6, s18
	s_sext_i32_i16 s6, s6
	s_and_b32 s18, s20, 0xffffffc0
	s_lshl_b32 s20, s6, 5
	v_ashrrev_i32_e32 v7, 5, v6
	s_ashr_i32 s21, s20, 31
	s_lshl_b64 s[46:47], s[20:21], 2
	v_add_u32_e32 v4, s18, v7
	v_and_b32_e32 v24, 31, v6
	s_add_u32 s46, s48, s46
	s_addc_u32 s47, s19, s47
	v_lshlrev_b32_e32 v0, 2, v24
	v_lshl_add_u32 v2, v7, 13, v0
	s_lshl_b32 s98, s18, 13
	s_add_u32 s100, s46, s98
	s_addc_u32 s101, s47, 0
	global_load_dword v25, v2, s[100:101]
	s_add_u32 s100, s100, 0x4000
	s_addc_u32 s101, s101, 0
	global_load_dword v26, v2, s[100:101]
	s_add_u32 s100, s100, 0x4000
	s_addc_u32 s101, s101, 0
	global_load_dword v27, v2, s[100:101]
	s_add_u32 s100, s100, 0x4000
	s_addc_u32 s101, s101, 0
	global_load_dword v28, v2, s[100:101]
	s_add_u32 s100, s100, 0x4000
	s_addc_u32 s101, s101, 0
	global_load_dword v29, v2, s[100:101]
	s_add_u32 s100, s100, 0x4000
	s_addc_u32 s101, s101, 0
	global_load_dword v30, v2, s[100:101]
	s_add_u32 s100, s100, 0x4000
	s_addc_u32 s101, s101, 0
	global_load_dword v31, v2, s[100:101]
	s_add_u32 s100, s100, 0x4000
	s_addc_u32 s101, s101, 0
	global_load_dword v32, v2, s[100:101]
	s_add_u32 s100, s100, 0x4000
	s_addc_u32 s101, s101, 0
	global_load_dword v33, v2, s[100:101]
	s_add_u32 s100, s100, 0x4000
	s_addc_u32 s101, s101, 0
	global_load_dword v34, v2, s[100:101]
	s_add_u32 s100, s100, 0x4000
	s_addc_u32 s101, s101, 0
	global_load_dword v35, v2, s[100:101]
	s_add_u32 s100, s100, 0x4000
	s_addc_u32 s101, s101, 0
	global_load_dword v36, v2, s[100:101]
	s_add_u32 s100, s100, 0x4000
	s_addc_u32 s101, s101, 0
	global_load_dword v37, v2, s[100:101]
	s_add_u32 s100, s100, 0x4000
	s_addc_u32 s101, s101, 0
	global_load_dword v38, v2, s[100:101]
	s_add_u32 s100, s100, 0x4000
	s_addc_u32 s101, s101, 0
	global_load_dword v39, v2, s[100:101]
	s_add_u32 s100, s100, 0x4000
	s_addc_u32 s101, s101, 0
	global_load_dword v40, v2, s[100:101]
	s_add_u32 s100, s100, 0x4000
	s_addc_u32 s101, s101, 0
	global_load_dword v41, v2, s[100:101]
	s_add_u32 s100, s100, 0x4000
	s_addc_u32 s101, s101, 0
	global_load_dword v42, v2, s[100:101]
	s_add_u32 s100, s100, 0x4000
	s_addc_u32 s101, s101, 0
	global_load_dword v43, v2, s[100:101]
	s_add_u32 s100, s100, 0x4000
	s_addc_u32 s101, s101, 0
	global_load_dword v44, v2, s[100:101]
	s_add_u32 s100, s100, 0x4000
	s_addc_u32 s101, s101, 0
	global_load_dword v45, v2, s[100:101]
	s_add_u32 s100, s100, 0x4000
	s_addc_u32 s101, s101, 0
	global_load_dword v46, v2, s[100:101]
	s_add_u32 s100, s100, 0x4000
	s_addc_u32 s101, s101, 0
	global_load_dword v20, v2, s[100:101]
	s_add_u32 s100, s100, 0x4000
	s_addc_u32 s101, s101, 0
	global_load_dword v21, v2, s[100:101]
	s_add_u32 s100, s100, 0x4000
	s_addc_u32 s101, s101, 0
	global_load_dword v22, v2, s[100:101]
	s_add_u32 s100, s100, 0x4000
	s_addc_u32 s101, s101, 0
	global_load_dword v10, v2, s[100:101]
	s_add_u32 s100, s100, 0x4000
	s_addc_u32 s101, s101, 0
	global_load_dword v11, v2, s[100:101]
	s_add_u32 s100, s100, 0x4000
	s_addc_u32 s101, s101, 0
	global_load_dword v12, v2, s[100:101]
	s_add_u32 s100, s100, 0x4000
	s_addc_u32 s101, s101, 0
	global_load_dword v13, v2, s[100:101]
	s_add_u32 s100, s100, 0x4000
	s_addc_u32 s101, s101, 0
	global_load_dword v14, v2, s[100:101]
	s_add_u32 s100, s100, 0x4000
	s_addc_u32 s101, s101, 0
	global_load_dword v4, v2, s[100:101]
	s_add_u32 s100, s100, 0x4000
	s_addc_u32 s101, s101, 0
	global_load_dword v5, v2, s[100:101]
	v_add_u32_e32 v0, s23, v0
	v_mad_u64_u32 v[2:3], s[46:47], v7, s40, v[0:1]
	s_waitcnt vmcnt(31)
	v_mul_f32_e32 v8, 0x42800000, v25
	s_waitcnt vmcnt(30)
	v_mul_f32_e32 v3, 0x42800000, v26
	ds_write2_b32 v2, v8, v3 offset1:66
	s_waitcnt vmcnt(29)
	v_mul_f32_e32 v3, 0x42800000, v27
	s_waitcnt vmcnt(28)
	v_mul_f32_e32 v7, 0x42800000, v28
	ds_write2_b32 v2, v3, v7 offset0:132 offset1:198
	s_waitcnt vmcnt(27)
	v_mul_f32_e32 v3, 0x42800000, v29
	s_waitcnt vmcnt(26)
	v_mul_f32_e32 v7, 0x42800000, v30
	v_add_u32_e32 v8, 0x400, v2
	ds_write2_b32 v8, v3, v7 offset0:8 offset1:74
	s_waitcnt vmcnt(25)
	v_mul_f32_e32 v3, 0x42800000, v31
	s_waitcnt vmcnt(24)
	v_mul_f32_e32 v7, 0x42800000, v32
	ds_write2_b32 v8, v3, v7 offset0:140 offset1:206
	s_waitcnt vmcnt(23)
	v_mul_f32_e32 v3, 0x42800000, v33
	s_waitcnt vmcnt(22)
	v_mul_f32_e32 v7, 0x42800000, v34
	v_add_u32_e32 v8, 0x800, v2
	ds_write2_b32 v8, v3, v7 offset0:16 offset1:82
	s_waitcnt vmcnt(21)
	v_mul_f32_e32 v3, 0x42800000, v35
	s_waitcnt vmcnt(20)
	v_mul_f32_e32 v7, 0x42800000, v36
	ds_write2_b32 v8, v3, v7 offset0:148 offset1:214
	s_waitcnt vmcnt(19)
	v_mul_f32_e32 v3, 0x42800000, v37
	s_waitcnt vmcnt(18)
	v_mul_f32_e32 v7, 0x42800000, v38
	v_add_u32_e32 v8, 0xc00, v2
	ds_write2_b32 v8, v3, v7 offset0:24 offset1:90
	s_waitcnt vmcnt(17)
	v_mul_f32_e32 v3, 0x42800000, v39
	s_waitcnt vmcnt(16)
	v_mul_f32_e32 v7, 0x42800000, v40
	ds_write2_b32 v8, v3, v7 offset0:156 offset1:222
	v_add_u32_e32 v8, 0x1000, v2
	s_ashr_i32 s19, s18, 31
	s_waitcnt vmcnt(15)
	v_mul_f32_e32 v3, 0x42800000, v41
	s_waitcnt vmcnt(14)
	v_mul_f32_e32 v7, 0x42800000, v42
	ds_write2_b32 v8, v3, v7 offset0:32 offset1:98
	s_waitcnt vmcnt(13)
	v_mul_f32_e32 v3, 0x42800000, v43
	s_waitcnt vmcnt(12)
	v_mul_f32_e32 v7, 0x42800000, v44
	ds_write2_b32 v8, v3, v7 offset0:164 offset1:230
	s_waitcnt vmcnt(11)
	v_mul_f32_e32 v3, 0x42800000, v45
	s_waitcnt vmcnt(10)
	v_mul_f32_e32 v7, 0x42800000, v46
	v_add_u32_e32 v8, 0x1400, v2
	ds_write2_b32 v8, v3, v7 offset0:40 offset1:106
	s_waitcnt vmcnt(9)
	v_mul_f32_e32 v3, 0x42800000, v20
	s_waitcnt vmcnt(8)
	v_mul_f32_e32 v7, 0x42800000, v21
	ds_write2_b32 v8, v3, v7 offset0:172 offset1:238
	v_add_u32_e32 v8, 0x1800, v2
	v_add_u32_e32 v2, 0x1c00, v2
	s_waitcnt vmcnt(7)
	v_mul_f32_e32 v3, 0x42800000, v22
	s_waitcnt vmcnt(6)
	v_mul_f32_e32 v7, 0x42800000, v10
	ds_write2_b32 v8, v3, v7 offset0:48 offset1:114
	s_waitcnt vmcnt(5)
	v_mul_f32_e32 v3, 0x42800000, v11
	s_waitcnt vmcnt(4)
	v_mul_f32_e32 v7, 0x42800000, v12
	ds_write2_b32 v8, v3, v7 offset0:180 offset1:246
	s_waitcnt vmcnt(3)
	v_mul_f32_e32 v3, 0x42800000, v13
	s_waitcnt vmcnt(2)
	v_mul_f32_e32 v7, 0x42800000, v14
	ds_write2_b32 v2, v3, v7 offset0:56 offset1:122
	v_and_b32_e32 v10, 0xffffffe0, v6
	v_mad_u64_u32 v[8:9], s[46:47], v10, s40, v[0:1]
	s_waitcnt vmcnt(1)
	v_mul_f32_e32 v3, 0x42800000, v4
	s_waitcnt vmcnt(0)
	v_mul_f32_e32 v4, 0x42800000, v5
	ds_write2_b32 v2, v3, v4 offset0:188 offset1:254
	s_waitcnt lgkmcnt(0)
	ds_read2_b32 v[2:3], v8 offset1:33
	ds_read2_b32 v[4:5], v8 offset0:66 offset1:99
	ds_read2_b32 v[6:7], v8 offset0:132 offset1:165
	s_waitcnt lgkmcnt(2)
	v_med3_f32 v0, v2, s39, v162
	v_med3_f32 v3, v3, s39, v162
	v_mov_b32_e32 v2, v1
	v_cvt_pk_fp8_f32 v2, v0, v3
	s_waitcnt lgkmcnt(1)
	v_med3_f32 v0, v4, s39, v162
	v_med3_f32 v3, v5, s39, v162
	ds_read2_b32 v[4:5], v8 offset0:198 offset1:231
	v_cvt_pk_fp8_f32 v2, v0, v3 op_sel:[0,0,1]
	s_waitcnt lgkmcnt(1)
	v_med3_f32 v0, v6, s39, v162
	v_med3_f32 v6, v7, s39, v162
	v_mov_b32_e32 v3, v1
	v_cvt_pk_fp8_f32 v3, v0, v6
	v_add_u32_e32 v0, 0x400, v8
	ds_read2_b32 v[6:7], v0 offset0:8 offset1:41
	s_waitcnt lgkmcnt(1)
	v_med3_f32 v4, v4, s39, v162
	v_med3_f32 v5, v5, s39, v162
	v_cvt_pk_fp8_f32 v3, v4, v5 op_sel:[0,0,1]
	ds_read2_b32 v[12:13], v0 offset0:74 offset1:107
	s_waitcnt lgkmcnt(1)
	v_med3_f32 v5, v6, s39, v162
	v_med3_f32 v6, v7, s39, v162
	v_mov_b32_e32 v4, v1
	v_cvt_pk_fp8_f32 v4, v5, v6
	ds_read2_b32 v[6:7], v0 offset0:140 offset1:173
	s_waitcnt lgkmcnt(1)
	v_med3_f32 v5, v12, s39, v162
	v_med3_f32 v9, v13, s39, v162
	v_cvt_pk_fp8_f32 v4, v5, v9 op_sel:[0,0,1]
	ds_read2_b32 v[12:13], v0 offset0:206 offset1:239
	s_waitcnt lgkmcnt(1)
	v_med3_f32 v0, v6, s39, v162
	v_med3_f32 v6, v7, s39, v162
	v_mov_b32_e32 v5, v1
	v_cvt_pk_fp8_f32 v5, v0, v6
	v_add_u32_e32 v0, 0x800, v8
	ds_read2_b32 v[6:7], v0 offset0:16 offset1:49
	s_waitcnt lgkmcnt(1)
	v_med3_f32 v9, v12, s39, v162
	v_med3_f32 v11, v13, s39, v162
	ds_read2_b32 v[12:13], v0 offset0:82 offset1:115
	v_cvt_pk_fp8_f32 v5, v9, v11 op_sel:[0,0,1]
	s_waitcnt lgkmcnt(1)
	v_med3_f32 v9, v6, s39, v162
	v_med3_f32 v7, v7, s39, v162
	v_mov_b32_e32 v6, v1
	ds_read2_b32 v[14:15], v0 offset0:148 offset1:181
	v_cvt_pk_fp8_f32 v6, v9, v7
	s_waitcnt lgkmcnt(1)
	v_med3_f32 v7, v12, s39, v162
	v_med3_f32 v9, v13, s39, v162
	ds_read2_b32 v[12:13], v0 offset0:214 offset1:247
	v_cvt_pk_fp8_f32 v6, v7, v9 op_sel:[0,0,1]
	s_waitcnt lgkmcnt(1)
	v_med3_f32 v0, v14, s39, v162
	v_med3_f32 v9, v15, s39, v162
	v_mov_b32_e32 v7, v1
	v_cvt_pk_fp8_f32 v7, v0, v9
	v_add_u32_e32 v0, 0xc00, v8
	ds_read2_b32 v[8:9], v0 offset0:24 offset1:57
	s_waitcnt lgkmcnt(1)
	v_med3_f32 v11, v12, s39, v162
	ds_read2_b32 v[14:15], v0 offset0:90 offset1:123
	v_med3_f32 v12, v13, s39, v162
	v_cvt_pk_fp8_f32 v7, v11, v12 op_sel:[0,0,1]
	ds_read2_b32 v[12:13], v0 offset0:156 offset1:189
	s_waitcnt lgkmcnt(2)
	v_med3_f32 v11, v8, s39, v162
	v_med3_f32 v9, v9, s39, v162
	s_waitcnt lgkmcnt(1)
	v_med3_f32 v16, v14, s39, v162
	v_med3_f32 v17, v15, s39, v162
	v_mov_b32_e32 v8, v1
	ds_read2_b32 v[14:15], v0 offset0:222 offset1:255
	v_cvt_pk_fp8_f32 v8, v11, v9
	s_waitcnt lgkmcnt(1)
	v_med3_f32 v0, v12, s39, v162
	v_med3_f32 v11, v13, s39, v162
	v_mov_b32_e32 v9, v1
	v_cvt_pk_fp8_f32 v9, v0, v11
	v_or_b32_e32 v12, s20, v24
	v_ashrrev_i32_e32 v13, 31, v12
	s_waitcnt lgkmcnt(0)
	v_med3_f32 v0, v14, s39, v162
	v_med3_f32 v11, v15, s39, v162
	v_lshlrev_b64 v[12:13], 10, v[12:13]
	v_cvt_pk_fp8_f32 v8, v16, v17 op_sel:[0,0,1]
	v_cvt_pk_fp8_f32 v9, v0, v11 op_sel:[0,0,1]
	v_lshl_add_u64 v[12:13], s[2:3], 0, v[12:13]
	v_lshl_add_u64 v[12:13], v[12:13], 0, s[18:19]
	v_ashrrev_i32_e32 v11, 31, v10
	v_lshl_add_u64 v[10:11], v[12:13], 0, v[10:11]
	global_store_dwordx4 v[10:11], v[2:5], off
	global_store_dwordx4 v[10:11], v[6:9], off offset:16
	s_waitcnt lgkmcnt(0)
	s_branch .LBB0_1472
